# v26 + attention start: rel_bias max loads batched under one wait (was 3 serialized round trips, twice per layer)
# baseline (speedup 1.0000x reference)
;     ...
;     { const int l64 = tid & 63;
;       float g0 = fabsf(a.in[I_QGF][layer * 64 + l64]), g1 = fabsf(a.in[I_KGF][layer * 64 + l64]), g2 = fabsf(a.in[I_QGD][layer * 64 + l64]), g3 = fabsf(a.in[I_KGD][layer * 64 + l64]);
;       float rbm = 0.f;
;       for (int i = l64; i < 32 * 6; i += 64) rbm = fmaxf(rbm, a.in[I_RELB][i]);
; #pragma unroll
;       for (int o2 = 1; o2 < 64; o2 <<= 1) { g0 = fmaxf(g0, __shfl_xor(g0, o2)); g1 = fmaxf(g1, __shfl_xor(g1, o2)); g2 = fmaxf(g2, __shfl_xor(g2, o2)); g3 = fmaxf(g3, __shfl_xor(g3, o2)); rbm = fmaxf(rbm, __shfl_xor(rbm, o2)); }
;       bfox = 8.f * g0 * g1 * LOG2E * 1.01f; bdil = 8.f * g2 * g3 * LOG2E * 1.01f; bmax = fmaxf(rbm, 0.f) * LOG2E; }
.LBB0_393:
	global_load_dword v9, v[2:3], off
	global_load_dword v10, v[2:3], off offset:256
	global_load_dword v11, v[2:3], off offset:512
	v_max_f32_e32 v7, v7, v7
	s_waitcnt vmcnt(0)
	v_max_f32_e32 v9, v9, v9
	v_max_f32_e32 v7, v7, v9
	v_max_f32_e32 v10, v10, v10
	v_max_f32_e32 v7, v7, v10
	v_max_f32_e32 v11, v11, v11
	v_max_f32_e32 v7, v7, v11
	s_or_b64 exec, exec, s[4:5]
	v_xor_b32_e32 v3, 1, v199
	v_cmp_lt_i32_e32 vcc, v3, v241
	v_and_b32_e32 v2, 0x7fffffff, v6
	v_and_b32_e32 v8, 0x7fffffff, v1
	v_cndmask_b32_e32 v3, v199, v3, vcc
	v_lshlrev_b32_e32 v156, 2, v3
	ds_bpermute_b32 v2, v156, v2
	v_and_b32_e32 v3, 0x7fffffff, v5
	ds_bpermute_b32 v3, v156, v3
	v_max_f32_e64 v6, |v6|, |v6|
	v_and_b32_e32 v9, 0x7fffffff, v4
	s_waitcnt lgkmcnt(1)
	v_max_f32_e32 v2, v2, v2
	v_max_f32_e32 v2, v6, v2
	ds_bpermute_b32 v6, v156, v8
	ds_bpermute_b32 v8, v156, v9
	s_waitcnt lgkmcnt(2)
	v_max_f32_e32 v3, v3, v3
	v_max_f32_e64 v5, |v5|, |v5|
	v_max_f32_e32 v3, v5, v3
	s_waitcnt lgkmcnt(1)
	v_max_f32_e32 v5, v6, v6
	v_max_f32_e64 v1, |v1|, |v1|
	v_max_f32_e32 v1, v1, v5
	s_waitcnt lgkmcnt(0)
	v_max_f32_e32 v5, v8, v8
	v_max_f32_e64 v4, |v4|, |v4|
	v_max_f32_e32 v4, v4, v5
	ds_bpermute_b32 v5, v156, v7
	v_xor_b32_e32 v6, 2, v199
	v_cmp_lt_i32_e32 vcc, v6, v241
	v_max_f32_e32 v7, v7, v7
	v_readlane_b32 s4, v255, 13
	v_cndmask_b32_e32 v6, v199, v6, vcc
	v_lshlrev_b32_e32 v158, 2, v6
	s_waitcnt lgkmcnt(0)
	v_max_f32_e32 v5, v5, v5
	v_max_f32_e32 v5, v7, v5
	ds_bpermute_b32 v7, v158, v3
	ds_bpermute_b32 v6, v158, v2
	ds_bpermute_b32 v8, v158, v1
	v_readlane_b32 s5, v255, 14
	s_ashr_i32 s18, s12, 6
	s_waitcnt lgkmcnt(2)
	v_max_f32_e32 v7, v7, v7
	s_waitcnt lgkmcnt(1)
	v_max_f32_e32 v6, v6, v6
	v_max_f32_e32 v3, v3, v7
	s_waitcnt lgkmcnt(0)
	v_max_f32_e32 v7, v8, v8
	v_xor_b32_e32 v8, 4, v199
	v_max_f32_e32 v2, v2, v6
	ds_bpermute_b32 v6, v158, v4
	v_cmp_lt_i32_e32 vcc, v8, v241
	v_max_f32_e32 v1, v1, v7
	ds_bpermute_b32 v7, v158, v5
	v_cndmask_b32_e32 v8, v199, v8, vcc
	v_lshlrev_b32_e32 v159, 2, v8
	ds_bpermute_b32 v8, v159, v2
	s_waitcnt lgkmcnt(2)
	v_max_f32_e32 v6, v6, v6
	v_max_f32_e32 v4, v4, v6
	s_waitcnt lgkmcnt(1)
	v_max_f32_e32 v6, v7, v7
	v_max_f32_e32 v5, v5, v6
	ds_bpermute_b32 v6, v159, v3
	s_waitcnt lgkmcnt(1)
	v_max_f32_e32 v7, v8, v8
	ds_bpermute_b32 v8, v159, v1
	v_max_f32_e32 v2, v2, v7
	ds_bpermute_b32 v7, v159, v4
	s_waitcnt lgkmcnt(2)
	v_max_f32_e32 v6, v6, v6
	v_max_f32_e32 v3, v3, v6
	s_waitcnt lgkmcnt(1)
	v_max_f32_e32 v6, v8, v8
	v_xor_b32_e32 v8, 8, v199
	v_cmp_lt_i32_e32 vcc, v8, v241
	v_max_f32_e32 v1, v1, v6
	s_waitcnt lgkmcnt(0)
	v_max_f32_e32 v6, v7, v7
	ds_bpermute_b32 v7, v159, v5
	v_cndmask_b32_e32 v8, v199, v8, vcc
	v_lshlrev_b32_e32 v160, 2, v8
	ds_bpermute_b32 v8, v160, v2
	v_max_f32_e32 v4, v4, v6
	s_waitcnt lgkmcnt(1)
	v_max_f32_e32 v6, v7, v7
	v_max_f32_e32 v5, v5, v6
	ds_bpermute_b32 v6, v160, v3
	s_waitcnt lgkmcnt(1)
	v_max_f32_e32 v7, v8, v8
	ds_bpermute_b32 v8, v160, v1
	v_max_f32_e32 v2, v2, v7
	ds_bpermute_b32 v7, v160, v4
	s_waitcnt lgkmcnt(2)
	v_max_f32_e32 v6, v6, v6
	v_max_f32_e32 v3, v3, v6
	s_waitcnt lgkmcnt(1)
	v_max_f32_e32 v6, v8, v8
	v_max_f32_e32 v1, v1, v6
	s_waitcnt lgkmcnt(0)
	v_max_f32_e32 v6, v7, v7
	ds_bpermute_b32 v7, v160, v5
	v_cmp_lt_i32_e32 vcc, v236, v241
	v_max_f32_e32 v4, v4, v6
	s_waitcnt lgkmcnt(0)
	v_max_f32_e32 v6, v7, v7
	v_cndmask_b32_e32 v8, v199, v236, vcc
	v_lshlrev_b32_e32 v250, 2, v8
	ds_bpermute_b32 v8, v250, v2
	ds_bpermute_b32 v7, v250, v3
	v_max_f32_e32 v5, v5, v6
	v_cmp_lt_i32_e32 vcc, v237, v241
	s_waitcnt lgkmcnt(1)
	v_max_f32_e32 v6, v8, v8
	v_max_f32_e32 v6, v2, v6
	ds_bpermute_b32 v2, v250, v1
	s_waitcnt lgkmcnt(1)
	v_max_f32_e32 v7, v7, v7
	ds_bpermute_b32 v8, v250, v4
	v_max_f32_e32 v7, v3, v7
	ds_bpermute_b32 v3, v250, v5
	s_waitcnt lgkmcnt(2)
	v_max_f32_e32 v2, v2, v2
	v_max_f32_e32 v9, v1, v2
	s_waitcnt lgkmcnt(1)
	v_max_f32_e32 v1, v8, v8
	v_max_f32_e32 v8, v4, v1
	s_waitcnt lgkmcnt(0)
	v_max_f32_e32 v1, v3, v3
	v_cndmask_b32_e32 v2, v199, v237, vcc
	v_max_f32_e32 v1, v5, v1
	v_lshlrev_b32_e32 v251, 2, v2
	ds_bpermute_b32 v14, v251, v6
	ds_bpermute_b32 v13, v251, v7
	ds_bpermute_b32 v12, v251, v9
	ds_bpermute_b32 v11, v251, v8
	ds_bpermute_b32 v10, v251, v1
	s_and_b64 vcc, exec, s[4:5]
	s_cbranch_vccz .LBB0_409
; #define LAS __attribute__((address_space(3)))
; #define FOX_ISSUE(i) do { const int j_ = jhi - (i), bf_ = (i) & 3; dma_kv(lds, bf_, Kb + (size_t)j_ * 4096, Vb + (size_t)j_ * 4096, 64, wid, lane); \
;         glds4(cum + j_ * 64 + lane, (unsigned)__builtin_amdgcn_readfirstlane(l0 + L_CK + bf_ * 256)); } while (0)
; __device__ __forceinline__ void dma_kv(LAS unsigned char* lds, int buf, const bf16_t* Kt, const bf16_t* Vt, size_t rowstride, int wid, int lane) {
;     const int krow = 8 * wid + (lane >> 3), kch = (lane & 7) ^ ((krow >> 1) & 7);
;     const bf16_t* ks = Kt + (size_t)krow * rowstride + kch * 8;
;     const bf16_t* vs = Vt + (size_t)(16 * (wid & 3) + (lane >> 2)) * rowstride + (wid >> 2) * 32 + (lane & 3) * 8;
;     const unsigned l0 = (unsigned)(uintptr_t)lds;
;     glds16(ks, (unsigned)__builtin_amdgcn_readfirstlane(l0 + L_K + buf * 8192 + wid * 1024));
;     glds16(vs, (unsigned)__builtin_amdgcn_readfirstlane(l0 + L_V + buf * 8192 + wid * 1024));
; }
;     ...
;     auto prologue = [&](int u) {
;         if (!UNIT_ON(u)) return;
;         int lane = tid & 63; asm volatile("" : "+v"(lane));
;         const int r32 = lane & 31, hi = lane >> 5;
;         if (u < AT_NFOX) {
;             const int qb = 15 - (u >> 5), bh = u & 31, b = bh >> 2, h = bh & 3, q0 = qb * 256;
;             const size_t rb = (size_t)b * S;
;             const bf16_t* Kb = proj + ((size_t)(4 + h) * NTOK + rb) * 64;
;             const bf16_t* Vb = proj + ((size_t)(8 + h) * NTOK + rb) * 64;
;             const float* cum = cumall + (size_t)bh * S;
;             const int jhi = 4 * qb + 3;
;             fox_cr = cum[q0]; fox_cv = cum[64 * (lane <= jhi ? lane : jhi) + 63]; fox_cq = cum[q0 + 32 * wid + r32];
;             if (!(dbg & 1)) { FOX_ISSUE(0); FOX_ISSUE(1); FOX_ISSUE(2); }
;             const bf16_t* Q = proj + ((size_t)(0 + h) * NTOK + rb + q0 + 32 * wid + r32) * 64;
; #pragma unroll
;             for (int d0 = 0; d0 < 4; ++d0) qr[d0] = *(const bf16x8*)(Q + d0 * 16 + hi * 8);
	v_readlane_b32 s6, v255, 15
	v_mov_b32_e32 v2, v157
	v_readlane_b32 s7, v255, 16
	s_mov_b64 s[4:5], -1
	v_and_b32_e32 v15, 31, v2
	s_and_b64 vcc, exec, s[6:7]
	s_cbranch_vccz .LBB0_407
	v_readlane_b32 s6, v255, 17
	v_readlane_b32 s7, v255, 18
	s_and_b64 vcc, exec, s[6:7]
	s_cbranch_vccz .LBB0_398
	s_lshl_b32 s2, s18, 3
	v_ashrrev_i32_e32 v3, 3, v2
	v_add_u32_e32 v4, s2, v3
	v_lshrrev_b32_e32 v3, 1, v4
	v_xor_b32_e32 v3, v3, v2
	v_ashrrev_i32_e32 v5, 31, v4
	v_readlane_b32 s4, v255, 19
	v_lshlrev_b64 v[4:5], 7, v[4:5]
	v_readlane_b32 s5, v255, 20
	v_lshlrev_b32_e32 v3, 4, v3
	v_and_b32_e32 v34, 0x70, v3
	v_lshl_add_u64 v[16:17], s[4:5], 0, v[4:5]
	s_lshl_b32 s4, s18, 4
	v_lshl_add_u64 v[20:21], v[16:17], 0, v[34:35]
	s_and_b32 s4, s4, 48
	v_ashrrev_i32_e32 v16, 2, v2
	v_add_u32_e32 v22, s4, v16
	v_ashrrev_i32_e32 v23, 31, v22
	v_readlane_b32 s4, v255, 21
	v_lshlrev_b64 v[22:23], 7, v[22:23]
	v_readlane_b32 s5, v255, 22
	v_lshlrev_b32_e32 v3, 4, v2
	v_and_b32_e32 v26, 48, v3
	v_lshl_add_u64 v[24:25], s[4:5], 0, v[22:23]
	s_and_b32 s4, s2, 0xffffffe0
	s_ashr_i32 s5, s4, 31
	s_lshl_b64 s[4:5], s[4:5], 1
	s_lshl_b32 s2, s18, 10
	v_lshl_add_u64 v[24:25], v[24:25], 0, s[4:5]
	v_mov_b32_e32 v27, v35
	s_add_i32 s2, s2, 0
	s_mov_b32 s6, m0
	s_mov_b32 m0, s2
	s_nop 0
	global_load_lds_dwordx4 v[20:21], off
	s_mov_b32 m0, s6
	v_lshl_add_u64 v[24:25], v[24:25], 0, v[26:27]
	s_add_i32 s6, s2, 0xc000
	s_mov_b32 s7, m0
	s_mov_b32 m0, s6
	s_nop 0
	global_load_lds_dwordx4 v[24:25], off
	s_mov_b32 m0, s7
	s_nop 0
	v_readlane_b32 s6, v255, 23
	v_readlane_b32 s7, v255, 24
	s_nop 1
	v_lshl_add_u64 v[20:21], s[6:7], 0, v[4:5]
	v_readlane_b32 s6, v255, 25
	v_readlane_b32 s7, v255, 26
	v_lshl_add_u64 v[20:21], v[20:21], 0, v[34:35]
	s_nop 0
	v_lshl_add_u64 v[24:25], s[6:7], 0, v[22:23]
	v_lshl_add_u64 v[24:25], v[24:25], 0, s[4:5]
	s_add_i32 s6, s2, 0x2000
	s_mov_b32 s7, m0
	s_mov_b32 m0, s6
	s_nop 0
	global_load_lds_dwordx4 v[20:21], off
	s_mov_b32 m0, s7
	v_lshl_add_u64 v[24:25], v[24:25], 0, v[26:27]
	s_add_i32 s6, s2, 0xe000
	s_mov_b32 s7, m0
	s_mov_b32 m0, s6
	s_nop 0
	global_load_lds_dwordx4 v[24:25], off
	s_mov_b32 m0, s7
	s_nop 0
	v_readlane_b32 s6, v255, 27
	v_readlane_b32 s7, v255, 28
	s_nop 1
	v_lshl_add_u64 v[4:5], s[6:7], 0, v[4:5]
	v_readlane_b32 s6, v255, 29
	v_readlane_b32 s7, v255, 30
	v_lshl_add_u64 v[4:5], v[4:5], 0, v[34:35]
	s_nop 0
	v_lshl_add_u64 v[20:21], s[6:7], 0, v[22:23]
	v_lshl_add_u64 v[20:21], v[20:21], 0, s[4:5]
	s_add_i32 s4, s2, 0x4000
	s_mov_b32 s5, m0
	s_mov_b32 m0, s4
	s_nop 0
	global_load_lds_dwordx4 v[4:5], off
	s_mov_b32 m0, s5
	s_add_i32 s2, s2, 0x10000
	v_lshl_add_u64 v[20:21], v[20:21], 0, v[26:27]
	s_mov_b32 s4, m0
	s_mov_b32 m0, s2
	s_nop 0
	global_load_lds_dwordx4 v[20:21], off
	s_mov_b32 m0, s4
	s_lshl_b32 s2, s18, 5
	s_ashr_i32 s4, s2, 31
	v_readlane_b32 s5, v255, 31
	s_add_u32 s2, s2, s5
	s_addc_u32 s4, s4, 0
	v_or_b32_e32 v4, s2, v15
	v_mov_b32_e32 v5, s4
	s_mov_b64 s[4:5], 0

; __device__ __forceinline__ void at_dil(const Args& a, LAS unsigned char* lds, int layer) {
;     ...
;     { const int l64 = tid & 63;
;       float g2 = fabsf(a.in[I_QGD][layer * 64 + l64]), g3 = fabsf(a.in[I_KGD][layer * 64 + l64]);
;       float rbm = 0.f;
;       for (int i = l64; i < 32 * 6; i += 64) rbm = fmaxf(rbm, a.in[I_RELB][i]);
; #pragma unroll
;       for (int o2 = 1; o2 < 64; o2 <<= 1) { g2 = fmaxf(g2, __shfl_xor(g2, o2)); g3 = fmaxf(g3, __shfl_xor(g3, o2)); rbm = fmaxf(rbm, __shfl_xor(rbm, o2)); }
;       bdil = 8.f * g2 * g3 * LOG2E * 1.01f; bmax = fmaxf(rbm, 0.f) * LOG2E; }
;     const bool dil_fixed = (bdil + bmax) < 40.f;
;     const float m_dil = bdil + bmax;
;     const unsigned l0 = (unsigned)(uintptr_t)lds;
;     __syncthreads();
;     if (tid < 32 * 6) relb[tid] = a.in[I_RELB][tid] * LOG2E;
.LBB0_527:
	global_load_dword v8, v[2:3], off
	global_load_dword v9, v[2:3], off offset:256
	global_load_dword v10, v[2:3], off offset:512
	v_max_f32_e32 v6, v6, v6
	s_waitcnt vmcnt(0)
	v_max_f32_e32 v8, v8, v8
	v_max_f32_e32 v6, v6, v8
	v_max_f32_e32 v9, v9, v9
	v_max_f32_e32 v6, v6, v9
	v_max_f32_e32 v10, v10, v10
	v_max_f32_e32 v6, v6, v10
	s_or_b64 exec, exec, s[4:5]
	v_and_b32_e32 v2, 0x7fffffff, v5
	ds_bpermute_b32 v2, v156, v2
	v_and_b32_e32 v3, 0x7fffffff, v4
	ds_bpermute_b32 v3, v156, v3
	ds_bpermute_b32 v7, v156, v6
	v_max_f32_e64 v5, |v5|, |v5|
	s_waitcnt lgkmcnt(2)
	v_max_f32_e32 v2, v2, v2
	v_max_f32_e32 v2, v5, v2
	s_waitcnt lgkmcnt(1)
	v_max_f32_e32 v3, v3, v3
	v_max_f32_e64 v4, |v4|, |v4|
	v_max_f32_e32 v3, v4, v3
	ds_bpermute_b32 v4, v158, v2
	s_waitcnt lgkmcnt(1)
	v_max_f32_e32 v5, v7, v7
	v_max_f32_e32 v6, v6, v6
	ds_bpermute_b32 v7, v158, v3
	v_max_f32_e32 v5, v6, v5
	ds_bpermute_b32 v6, v158, v5
	s_waitcnt lgkmcnt(2)
	v_max_f32_e32 v4, v4, v4
	v_max_f32_e32 v2, v2, v4
	s_waitcnt lgkmcnt(1)
	v_max_f32_e32 v4, v7, v7
	ds_bpermute_b32 v7, v159, v2
	v_max_f32_e32 v3, v3, v4
	s_waitcnt lgkmcnt(1)
	v_max_f32_e32 v4, v6, v6
	ds_bpermute_b32 v6, v159, v3
	v_max_f32_e32 v4, v5, v4
	s_waitcnt lgkmcnt(1)
	v_max_f32_e32 v5, v7, v7
	ds_bpermute_b32 v7, v159, v4
	v_max_f32_e32 v2, v2, v5
	s_waitcnt lgkmcnt(1)
	v_max_f32_e32 v5, v6, v6
	ds_bpermute_b32 v6, v160, v2
	v_max_f32_e32 v3, v3, v5
	s_waitcnt lgkmcnt(1)
	v_max_f32_e32 v5, v7, v7
	ds_bpermute_b32 v7, v160, v3
	v_max_f32_e32 v4, v4, v5
	s_waitcnt lgkmcnt(1)
	v_max_f32_e32 v5, v6, v6
	ds_bpermute_b32 v6, v160, v4
	v_max_f32_e32 v2, v2, v5
	s_waitcnt lgkmcnt(1)
	v_max_f32_e32 v5, v7, v7
	v_max_f32_e32 v3, v3, v5
	ds_bpermute_b32 v5, v250, v2
	s_waitcnt lgkmcnt(1)
	v_max_f32_e32 v6, v6, v6
	ds_bpermute_b32 v7, v250, v3
	v_max_f32_e32 v6, v4, v6
	ds_bpermute_b32 v8, v250, v6
	s_waitcnt lgkmcnt(2)
	v_max_f32_e32 v4, v5, v5
	v_max_f32_e32 v2, v2, v4
	s_waitcnt lgkmcnt(1)
	v_max_f32_e32 v4, v7, v7
	v_max_f32_e32 v4, v3, v4
	s_waitcnt lgkmcnt(0)
	v_max_f32_e32 v3, v8, v8
	v_max_f32_e32 v5, v6, v3
	ds_bpermute_b32 v3, v251, v2
	ds_bpermute_b32 v6, v251, v4
	ds_bpermute_b32 v7, v251, v5
	s_movk_i32 s2, 0xc0
	v_cmp_gt_i32_e32 vcc, s2, v18
	s_waitcnt lgkmcnt(0)
	s_barrier
	s_and_saveexec_b64 s[4:5], vcc
	s_cbranch_execz .LBB0_530
	v_readlane_b32 s8, v252, 41
	v_ashrrev_i32_e32 v19, 31, v18
	v_readlane_b32 s9, v252, 42
	v_readlane_b32 s10, v252, 43
	v_readlane_b32 s11, v252, 44
	v_lshl_add_u64 v[8:9], v[18:19], 2, s[8:9]
	global_load_dword v8, v[8:9], off
	v_lshl_add_u32 v9, v18, 2, 0
	v_add_u32_e32 v9, 0x21f00, v9
	v_readlane_b32 s12, v252, 45
	v_readlane_b32 s13, v252, 46
	v_readlane_b32 s14, v252, 47
	v_readlane_b32 s15, v252, 48
	s_waitcnt vmcnt(0)
	v_mul_f32_e32 v8, 0x3fb8aa3b, v8
	ds_write_b32 v9, v8
